# n53_gemm_vm20
# baseline (speedup 1.0000x reference)
.LBB1_4:
	s_or_b64 exec, exec, s[28:29]
	s_cmp_lg_u32 s37, 0
	s_cbranch_scc0 .LBB1_13
	s_waitcnt vmcnt(20)
	s_cbranch_execnz .LBB1_7
